# speedup vs baseline: 1.0056x; 1.0056x over previous
_Z11knrm_kernelPKfS0_PKiS2_S0_Pf:
	s_load_dwordx8 s[4:11], s[0:1], 0x0
	s_load_dwordx4 s[12:15], s[0:1], 0x20
	v_lshrrev_b32_e32 v1, 6, v0
	v_and_b32_e32 v120, 63, v0
	v_lshrrev_b32_e32 v100, 4, v0
	v_and_b32_e32 v123, 15, v0
	v_lshlrev_b32_e32 v124, 5, v1
	s_lshl_b32 s3, s2, 5
	v_lshl_or_b32 v8, s2, 8, v124
	v_or_b32_e32 v2, s3, v100
	s_movk_i32 s3, 0x4b0
	v_mul_lo_u32 v2, v2, s3
	v_mul_lo_u32 v99, v8, s3
	v_lshlrev_b32_e32 v132, 4, v120
	v_min_u32_e32 v193, 23, v120
	v_lshl_add_u32 v3, v123, 4, v2
	v_min_u32_e32 v4, 10, v123
	v_add_u32_e32 v192, v99, v132
	v_lshlrev_b32_e32 v193, 4, v193
	s_movk_i32 s27, 0x1000
	s_movk_i32 s28, 0x2000
	v_lshl_add_u32 v2, v4, 4, v2
	v_add3_u32 v193, v99, v193, s28
	s_mov_b32 s19, 0x20000
	s_mov_b32 s18, 0x4b00000
	s_waitcnt lgkmcnt(0)
	s_mov_b64 s[16:17], s[6:7]
	s_and_b32 s5, s5, 0xffff
	s_mov_b32 s6, 0x960000
	s_mov_b32 s7, s19
	s_and_b32 s17, s17, 0xffff
	buffer_load_dwordx4 v[90:93], v3, s[4:7], 0 offen nt
	buffer_load_dwordx4 v[86:89], v3, s[4:7], 0 offen offset:256 nt
	buffer_load_dwordx4 v[82:85], v3, s[4:7], 0 offen offset:512 nt
	buffer_load_dwordx4 v[78:81], v3, s[4:7], 0 offen offset:768 nt
	buffer_load_dwordx4 v[94:97], v2, s[4:7], 0 offen offset:1024 nt
	buffer_load_dwordx4 v[2:5], v192, s[16:19], 0 offen nt
	buffer_load_dwordx4 v[14:17], v192, s[16:19], 0 offen offset:1024 nt
	buffer_load_dwordx4 v[34:37], v192, s[16:19], 0 offen offset:2048 nt
	buffer_load_dwordx4 v[46:49], v192, s[16:19], 0 offen offset:3072 nt
	buffer_load_dwordx4 v[54:57], v192, s[16:19], s27 offen nt
	buffer_load_dwordx4 v[58:61], v192, s[16:19], s27 offen offset:1024 nt
	buffer_load_dwordx4 v[62:65], v192, s[16:19], s27 offen offset:2048 nt
	buffer_load_dwordx4 v[66:69], v192, s[16:19], s27 offen offset:3072 nt
	buffer_load_dwordx4 v[70:73], v192, s[16:19], s28 offen nt
	buffer_load_dwordx4 v[74:77], v193, s[16:19], 0 offen offset:1024 nt
	v_lshlrev_b32_e32 v42, 2, v0
	v_bfe_u32 v43, v0, 2, 2
	v_and_or_b32 v98, v42, 12, v43
	v_and_b32_e32 v126, 7, v98
	v_and_b32_e32 v6, 31, v120
	v_or_b32_e32 v6, v6, v8
	v_ashrrev_i32_e32 v7, 31, v6
	s_movk_i32 s0, 0x160
	v_lshl_add_u64 v[6:7], v[6:7], 2, s[10:11]
	v_lshrrev_b32_e32 v121, 5, v0
	v_cmp_gt_u32_e64 s[0:1], s0, v0
	global_load_dword v125, v[6:7], off
	s_nop 0
	s_nop 0
	s_nop 0
	v_cndmask_b32_e64 v42, 10, v121, s[0:1]
	v_lshlrev_b32_e32 v42, 2, v42
	s_lshl_b32 s3, s2, 5
	v_and_b32_e32 v122, 31, v0
	global_load_dword v118, v42, s[12:13]
	v_or_b32_e32 v42, s3, v122
	v_ashrrev_i32_e32 v43, 31, v42
	v_lshl_add_u64 v[42:43], v[42:43], 2, s[8:9]
	global_load_dword v119, v[42:43], off
	s_mov_b32 s3, 0
	v_mul_u32_u24_e32 v131, 0x2600, v1
	v_cmp_gt_u32_e64 s[4:5], 16, v120
	s_and_saveexec_b64 s[6:7], s[4:5]
	s_movk_i32 s8, 0x260
	v_mov_b32_e32 v102, 0
	v_mad_u32_u24 v101, v120, s8, v131
	v_mov_b32_e32 v103, v102
	ds_write_b64 v101, v[102:103] offset:20056
	s_or_b64 exec, exec, s[6:7]
	v_cmp_lt_u32_e32 vcc, 10, v123
	s_waitcnt vmcnt(16)
	v_mul_f32_e32 v101, v87, v87
	v_mov_b32_e32 v106, v92
	s_waitcnt vmcnt(13)
	v_cndmask_b32_e64 v103, v97, 0, vcc
	v_cndmask_b32_e64 v102, v96, 0, vcc
	v_mov_b32_e32 v96, v91
	v_mov_b32_e32 v97, v83
	v_cndmask_b32_e64 v105, v95, 0, vcc
	v_cndmask_b32_e64 v104, v94, 0, vcc
	v_mov_b32_e32 v94, v90
	v_mov_b32_e32 v95, v82
	v_pk_mul_f32 v[96:97], v[96:97], v[96:97]
	v_mov_b32_e32 v107, v84
	v_fmac_f32_e32 v101, v86, v86
	v_pk_fma_f32 v[94:95], v[94:95], v[94:95], v[96:97]
	v_mov_b32_e32 v108, v93
	v_mov_b32_e32 v109, v85
	v_fmac_f32_e32 v101, v88, v88
	v_pk_fma_f32 v[94:95], v[106:107], v[106:107], v[94:95]
	v_fmac_f32_e32 v101, v89, v89
	v_pk_fma_f32 v[94:95], v[108:109], v[108:109], v[94:95]
	v_mov_b32_e32 v96, v79
	v_add_f32_e32 v94, v94, v101
	v_mov_b32_e32 v97, v105
	v_add_f32_e32 v101, v94, v95
	v_mov_b32_e32 v94, v78
	v_mov_b32_e32 v95, v104
	v_pk_mul_f32 v[96:97], v[96:97], v[96:97]
	s_mov_b32 s21, 0xf800000
	v_pk_fma_f32 v[94:95], v[94:95], v[94:95], v[96:97]
	v_mov_b32_e32 v96, v80
	v_mov_b32_e32 v97, v102
	v_pk_fma_f32 v[94:95], v[96:97], v[96:97], v[94:95]
	v_mov_b32_e32 v96, v81
	v_mov_b32_e32 v97, v103
	v_pk_fma_f32 v[94:95], v[96:97], v[96:97], v[94:95]
	v_mov_b32_e32 v135, 0x260
	v_add_f32_e32 v94, v101, v94
	v_add_f32_e32 v94, v94, v95
	v_mbcnt_lo_u32_b32 v95, -1, 0
	v_mbcnt_hi_u32_b32 v95, -1, v95
	v_and_b32_e32 v97, 64, v95
	v_add_u32_e32 v101, 64, v97
	s_movk_i32 s8, 0x260
	v_add_u32_e32 v137, 0x4b00, v99
	s_movk_i32 s10, 0x1b5
	v_mov_b32_e32 v99, 0x36a00
	v_mov_b32_e32 v111, 0x666c0
	v_mov_b32_e32 v113, 0x6d400
	v_mov_b32_e32 v115, 0x74140
	s_mov_b32 s20, 0xbeb17218
	s_mov_b32 s22, 0x44132d1f
	v_mov_b32_e32 v161, 0xc47a0000
	v_add_f32_dpp v96, v94, v94 quad_perm:[1,0,3,2] row_mask:0xf bank_mask:0xf
	s_nop 1
	v_add_f32_dpp v94, v96, v96 quad_perm:[2,3,0,1] row_mask:0xf bank_mask:0xf
	s_nop 1
	v_add_f32_dpp v96, v94, v94 row_half_mirror row_mask:0xf bank_mask:0xf
	s_nop 1
	v_add_f32_dpp v94, v96, v96 row_mirror row_mask:0xf bank_mask:0xf
	v_mul_f32_e32 v96, 0x4f800000, v94
	v_cmp_gt_f32_e32 vcc, s21, v94
	s_nop 1
	v_cndmask_b32_e32 v94, v94, v96, vcc
	v_sqrt_f32_e32 v96, v94
	s_nop 0
	v_add_u32_e32 v106, -1, v96
	v_fma_f32 v107, -v106, v96, v94
	v_cmp_ge_f32_e64 s[6:7], 0, v107
	v_add_u32_e32 v107, 1, v96
	s_nop 0
	v_cndmask_b32_e64 v106, v96, v106, s[6:7]
	v_fma_f32 v96, -v107, v96, v94
	v_cmp_lt_f32_e64 s[6:7], 0, v96
	s_nop 1
	v_cndmask_b32_e64 v96, v106, v107, s[6:7]
	v_mul_f32_e32 v106, 0x37800000, v96
	v_cndmask_b32_e32 v96, v96, v106, vcc
	v_cmp_class_f32_e32 vcc, v94, v135
	s_nop 1
	v_cndmask_b32_e32 v94, v96, v94, vcc
	v_add_f32_e32 v96, 0x29e12e13, v94
	v_div_scale_f32 v106, s[6:7], v96, v96, 1.0
	v_rcp_f32_e32 v107, v106
	v_mov_b32_e32 v94, 0
	v_cmp_gt_u32_e64 s[6:7], 48, v120
	v_mov_b32_e32 v116, v94
	v_fma_f32 v108, -v106, v107, 1.0
	v_fmac_f32_e32 v107, v108, v107
	v_div_scale_f32 v108, vcc, 1.0, v96, 1.0
	v_mul_f32_e32 v109, v108, v107
	v_fma_f32 v110, -v106, v109, v108
	v_fmac_f32_e32 v109, v110, v107
	v_fma_f32 v106, -v106, v109, v108
	v_div_fmas_f32 v106, v106, v107, v109
	v_div_fixup_f32 v96, v106, v96, 1.0
	v_lshlrev_b32_e32 v106, 3, v123
	v_pk_mul_f32 v[82:83], v[96:97], v[82:83] op_sel_hi:[0,1]
	v_pk_mul_f32 v[84:85], v[96:97], v[84:85] op_sel_hi:[0,1]
	v_pk_mul_f32 v[78:79], v[96:97], v[78:79] op_sel_hi:[0,1]
	v_pk_mul_f32 v[80:81], v[96:97], v[80:81] op_sel_hi:[0,1]
	v_mad_u32_u24 v100, v100, s8, v106
	v_cvt_pk_f16_f32 v82, v82, v83
	v_cvt_pk_f16_f32 v83, v84, v85
	v_cvt_pk_f16_f32 v78, v78, v79
	v_cvt_pk_f16_f32 v79, v80, v81
	ds_write2_b64 v100, v[82:83], v[78:79] offset0:32 offset1:48
	v_min_u32_e32 v82, 23, v120
	v_mov_b32_e32 v83, 0x2400
	v_lshl_or_b32 v138, v82, 4, v83
	v_xor_b32_e32 v83, 16, v95
	v_cmp_lt_i32_e32 vcc, v83, v101
	v_pk_mul_f32 v[90:91], v[96:97], v[90:91] op_sel_hi:[0,1]
	v_pk_mul_f32 v[92:93], v[96:97], v[92:93] op_sel_hi:[0,1]
	v_cndmask_b32_e32 v83, v95, v83, vcc
	v_lshlrev_b32_e32 v133, 2, v83
	v_xor_b32_e32 v83, 32, v95
	v_pk_mul_f32 v[86:87], v[96:97], v[86:87] op_sel_hi:[0,1]
	v_pk_mul_f32 v[88:89], v[96:97], v[88:89] op_sel_hi:[0,1]
	v_pk_mul_f32 v[78:79], v[96:97], v[104:105] op_sel_hi:[0,1]
	v_pk_mul_f32 v[80:81], v[96:97], v[102:103] op_sel_hi:[0,1]
	v_cmp_lt_i32_e32 vcc, v83, v101
	v_cvt_pk_f16_f32 v90, v90, v91
	v_cvt_pk_f16_f32 v91, v92, v93
	v_cvt_pk_f16_f32 v86, v86, v87
	v_cvt_pk_f16_f32 v87, v88, v89
	v_cvt_pk_f16_f32 v78, v78, v79
	v_cvt_pk_f16_f32 v79, v80, v81
	v_mov_b32_e32 v81, 0x17c00
	v_cndmask_b32_e32 v83, v95, v83, vcc
	ds_write2_b64 v100, v[90:91], v[86:87] offset1:16
	v_sub_u32_e64 v80, v123, 11 clamp
	v_lshl_or_b32 v81, v1, 7, v81
	v_lshlrev_b32_e32 v134, 2, v83
	v_or_b32_e32 v83, 64, v120
	v_mov_b32_e32 v86, 0x6d40
	v_mov_b32_e32 v87, 0xda80
	v_mov_b32_e32 v89, 0x147c0
	v_mov_b32_e32 v91, 0x1b500
	v_mov_b32_e32 v93, 0x28f80
	v_mov_b32_e32 v96, 0x2fcc0
	v_mov_b32_e32 v101, 0x3d740
	v_mov_b32_e32 v103, 0x44480
	v_mov_b32_e32 v105, 0x4b1c0
	v_mov_b32_e32 v107, 0x58c40
	v_or_b32_e32 v109, 0x3c0, v0
	v_mad_i32_i24 v80, v80, -8, v100
	v_lshrrev_b32_e32 v82, 1, v120
	v_lshl_add_u32 v139, v120, 2, v81
	v_and_or_b32 v140, v120, 48, v81
	v_lshlrev_b32_e32 v81, 3, v120
	v_mul_u32_u24_e32 v84, 0x1b5, v83
	v_lshl_add_u32 v85, v83, 3, v131
	v_mad_u32_u24 v86, v83, s10, v86
	v_mad_u32_u24 v87, v83, s10, v87
	v_mad_u32_u24 v89, v83, s10, v89
	v_mad_u32_u24 v91, v83, s10, v91
	v_mad_u32_u24 v93, v83, s10, v93
	v_mad_u32_u24 v96, v83, s10, v96
	v_mad_u32_u24 v99, v83, s10, v99
	v_mad_u32_u24 v101, v83, s10, v101
	v_mad_u32_u24 v103, v83, s10, v103
	v_mad_u32_u24 v105, v83, s10, v105
	v_mad_u32_u24 v107, v83, s10, v107
	v_mul_u32_u24_e32 v110, 0x1b5, v109
	v_mad_u32_u24 v111, v83, s10, v111
	v_mad_u32_u24 v113, v83, s10, v113
	v_mad_u32_u24 v83, v83, s10, v115
	ds_write_b64 v80, v[78:79] offset:512
	v_mul_u32_u24_e32 v78, 0x260, v123
	v_and_b32_e32 v82, 24, v82
	v_lshrrev_b32_e32 v84, 12, v84
	v_add_u32_e32 v141, v131, v81
	v_lshrrev_b32_e32 v86, 12, v86
	v_lshrrev_b32_e32 v87, 12, v87
	v_lshrrev_b32_e32 v89, 12, v89
	v_lshrrev_b32_e32 v91, 12, v91
	v_lshrrev_b32_e32 v93, 12, v93
	v_lshrrev_b32_e32 v96, 12, v96
	v_lshrrev_b32_e32 v99, 12, v99
	v_lshrrev_b32_e32 v101, 12, v101
	v_lshrrev_b32_e32 v103, 12, v103
	v_lshrrev_b32_e32 v105, 12, v105
	v_lshrrev_b32_e32 v107, 12, v107
	v_lshrrev_b32_e32 v110, 12, v110
	v_lshrrev_b32_e32 v111, 12, v111
	v_lshrrev_b32_e32 v113, 12, v113
	v_lshrrev_b32_e32 v83, 12, v83
	v_and_b32_e32 v79, 48, v0
	v_mad_u32_u24 v80, v98, s8, v131
	v_and_b32_e32 v84, 8, v84
	v_add_u32_e32 v81, 0x400, v141
	v_and_b32_e32 v86, 24, v86
	v_add_u32_e32 v88, 0x600, v141
	v_and_b32_e32 v87, 24, v87
	v_add_u32_e32 v90, 0x800, v141
	v_and_b32_e32 v89, 56, v89
	v_add_u32_e32 v92, 0xa00, v141
	v_and_b32_e32 v91, 56, v91
	v_add_u32_e32 v95, 0xe00, v141
	v_and_b32_e32 v93, 56, v93
	v_add_u32_e32 v98, 0x1000, v141
	v_and_b32_e32 v96, 56, v96
	v_add_u32_e32 v100, 0x1200, v141
	v_and_b32_e32 v99, 0x78, v99
	v_add_u32_e32 v102, 0x1400, v141
	v_and_b32_e32 v101, 0x78, v101
	v_add_u32_e32 v104, 0x1600, v141
	v_and_b32_e32 v103, 0x58, v103
	v_add_u32_e32 v106, 0x1800, v141
	v_and_b32_e32 v105, 0x58, v105
	v_add_u32_e32 v108, 0x1c00, v141
	v_and_b32_e32 v107, 0x78, v107
	v_lshl_add_u32 v109, v109, 3, v131
	v_and_b32_e32 v110, 0x78, v110
	v_add_u32_e32 v112, 0x2000, v141
	v_and_b32_e32 v111, 0x78, v111
	v_add_u32_e32 v114, 0x2200, v141
	v_and_b32_e32 v113, 0x78, v113
	v_add_u32_e32 v115, 0x2400, v141
	v_and_b32_e32 v83, 0xf8, v83
	s_movk_i32 s10, 0x4c00
	v_add_u32_e32 v78, v78, v82
	v_mad_u32_u24 v136, v123, s8, v79
	v_cmp_gt_u32_e64 s[8:9], 24, v120
	v_add3_u32 v142, v80, v79, s10
	v_add_u32_e32 v143, v85, v84
	v_add_u32_e32 v144, v81, v86
	v_add_u32_e32 v145, v88, v87
	v_add_u32_e32 v146, v90, v89
	v_add_u32_e32 v147, v92, v91
	v_add_u32_e32 v148, v95, v93
	v_add_u32_e32 v149, v98, v96
	v_add_u32_e32 v150, v100, v99
	v_add_u32_e32 v151, v102, v101
	v_add_u32_e32 v152, v104, v103
	v_add_u32_e32 v153, v106, v105
	v_add_u32_e32 v154, v108, v107
	v_add_u32_e32 v155, v109, v110
	v_add_u32_e32 v156, v112, v111
	v_add_u32_e32 v157, v114, v113
	v_add_u32_e32 v158, v115, v83
	v_add_u32_e32 v159, v80, v82
	v_add_u32_e32 v160, 64, v78
	v_mov_b32_e32 v96, 0xc604b4df
	v_mov_b32_e32 v95, v94
	v_mov_b32_e32 v98, v94
	v_mov_b32_e32 v99, v94
	v_mov_b32_e32 v100, v94
	v_mov_b32_e32 v101, v94
	v_mov_b32_e32 v102, v94
	v_mov_b32_e32 v103, v94
	v_mov_b32_e32 v104, v94
	v_mov_b32_e32 v105, v94
	v_mov_b32_e32 v106, v94
	v_mov_b32_e32 v107, v94
	v_mov_b32_e32 v108, v94
	v_mov_b32_e32 v109, v94
	v_mov_b32_e32 v110, v94
	v_mov_b32_e32 v111, v94
	v_mov_b32_e32 v112, v94
	v_mov_b32_e32 v113, v94
	v_mov_b32_e32 v114, v94
	v_mov_b32_e32 v115, v94
	v_mov_b32_e32 v117, v94
	s_waitcnt lgkmcnt(0)
	s_barrier
	s_mov_b32 s26, 0x2580
	s_mov_b32 s27, 0x3580
	s_mov_b32 s28, 0x4580
	buffer_load_dwordx4 v[6:9], v192, s[16:19], s26 offen nt
	buffer_load_dwordx4 v[10:13], v192, s[16:19], s26 offen offset:1024 nt
	buffer_load_dwordx4 v[18:21], v192, s[16:19], s26 offen offset:2048 nt
	buffer_load_dwordx4 v[22:25], v192, s[16:19], s26 offen offset:3072 nt
	buffer_load_dwordx4 v[26:29], v192, s[16:19], s27 offen nt
	buffer_load_dwordx4 v[30:33], v192, s[16:19], s27 offen offset:1024 nt
	buffer_load_dwordx4 v[38:41], v192, s[16:19], s27 offen offset:2048 nt
	buffer_load_dwordx4 v[42:45], v192, s[16:19], s27 offen offset:3072 nt
	buffer_load_dwordx4 v[50:53], v192, s[16:19], s28 offen nt
	buffer_load_dwordx4 v[186:189], v193, s[16:19], s26 offen offset:1024 nt
	s_waitcnt vmcnt(22)
	v_cvt_pk_f16_f32 v79, v4, v5
	v_cvt_pk_f16_f32 v78, v2, v3
	ds_write_b64 v141, v[78:79] offset:19456
	s_waitcnt vmcnt(21)
	v_cvt_pk_f16_f32 v79, v16, v17
	v_cvt_pk_f16_f32 v78, v14, v15
	ds_write_b64 v143, v[78:79] offset:19456
	s_waitcnt vmcnt(20)
	v_cvt_pk_f16_f32 v79, v36, v37
	v_cvt_pk_f16_f32 v78, v34, v35
	ds_write_b64 v144, v[78:79] offset:19456
	s_waitcnt vmcnt(19)
	v_cvt_pk_f16_f32 v79, v48, v49
	v_cvt_pk_f16_f32 v78, v46, v47
	ds_write_b64 v145, v[78:79] offset:19456
	s_waitcnt vmcnt(18)
	v_cvt_pk_f16_f32 v79, v56, v57
	v_cvt_pk_f16_f32 v78, v54, v55
	ds_write_b64 v146, v[78:79] offset:19456
	s_waitcnt vmcnt(17)
	v_cvt_pk_f16_f32 v79, v60, v61
	v_cvt_pk_f16_f32 v78, v58, v59
	ds_write_b64 v147, v[78:79] offset:19456
	s_waitcnt vmcnt(16)
	v_cvt_pk_f16_f32 v79, v64, v65
	v_cvt_pk_f16_f32 v78, v62, v63
	ds_write_b64 v141, v[78:79] offset:22568
	s_waitcnt vmcnt(15)
	v_cvt_pk_f16_f32 v79, v68, v69
	v_cvt_pk_f16_f32 v78, v66, v67
	ds_write_b64 v148, v[78:79] offset:19456
	s_waitcnt vmcnt(14)
	v_cvt_pk_f16_f32 v79, v72, v73
	v_cvt_pk_f16_f32 v78, v70, v71
	ds_write_b64 v149, v[78:79] offset:19456
	s_waitcnt vmcnt(13)
	v_cvt_pk_f16_f32 v79, v76, v77
	v_cvt_pk_f16_f32 v78, v74, v75
	s_and_saveexec_b64 s[12:13], s[8:9]
	ds_write_b64 v150, v[78:79] offset:19456
	s_or_b64 exec, exec, s[12:13]
	s_waitcnt vmcnt(10)
	v_cmp_lt_i32_e64 s[30:31], 1, v125
	s_nop 2
	v_lshrrev_b32_e64 v190, v126, s30
	v_and_b32_e32 v191, 1, v190
	v_lshrrev_b32_e32 v126, 7, v190
	v_lshrrev_b32_e32 v127, 14, v190
	v_lshrrev_b32_e32 v190, 21, v190
	v_and_b32_e32 v126, 2, v126
	v_and_b32_e32 v127, 4, v127
	v_and_b32_e32 v190, 8, v190
	v_or3_b32 v191, v191, v126, v127
	v_or_b32_e32 v191, v191, v190
	s_mov_b32 s26, 0x4b00
	s_mov_b32 s27, 0x5b00
	s_mov_b32 s28, 0x6b00
	buffer_load_dwordx4 v[2:5], v192, s[16:19], s26 offen nt
	buffer_load_dwordx4 v[14:17], v192, s[16:19], s26 offen offset:1024 nt
	buffer_load_dwordx4 v[34:37], v192, s[16:19], s26 offen offset:2048 nt
	buffer_load_dwordx4 v[46:49], v192, s[16:19], s26 offen offset:3072 nt
	buffer_load_dwordx4 v[54:57], v192, s[16:19], s27 offen nt
	buffer_load_dwordx4 v[58:61], v192, s[16:19], s27 offen offset:1024 nt
	buffer_load_dwordx4 v[62:65], v192, s[16:19], s27 offen offset:2048 nt
	buffer_load_dwordx4 v[66:69], v192, s[16:19], s27 offen offset:3072 nt
	buffer_load_dwordx4 v[70:73], v192, s[16:19], s28 offen nt
	buffer_load_dwordx4 v[74:77], v193, s[16:19], s26 offen offset:1024 nt
	s_mov_b32 s3, 0
	s_branch .LBB0_7
